# v16: v10 with progress published two rounds behind (store wait vmcnt 16/18 instead of 8/9)
# baseline (speedup 1.0000x reference)
.Lx14_w0:
	s_waitcnt vmcnt(18)

.LBB0_1726:
	s_add_i32 s0, s71, -2
	s_lshl_b32 s1, s83, 2
	s_add_i32 s1, s1, 0xc400
	v_cmp_eq_u32_e32 vcc, 0, v0
	v_mov_b32_e32 v18, s1
	v_mov_b32_e32 v19, s0
	s_and_saveexec_b64 s[0:1], vcc
	s_cbranch_execz .Lx14_pub_skip
	global_store_dword v18, v19, s[54:55] sc1
